# candidate exact-distance reduction: DPP row rotations instead of ds_bpermute butterfly
# speedup vs baseline: 1.0161x; 1.0051x over previous
.LBB0_445:
	s_or_b64 exec, exec, s[0:1]
	s_and_b64 s[16:17], s[6:7], vcc
	s_waitcnt lgkmcnt(0)
	s_nop 3
	v_mov_b32_dpp v68, v66 row_ror:8 row_mask:0xf bank_mask:0xf
	v_mov_b32_dpp v69, v67 row_ror:8 row_mask:0xf bank_mask:0xf
	v_add_f64 v[66:67], v[66:67], v[68:69]
	s_nop 1
	v_mov_b32_dpp v68, v66 row_ror:4 row_mask:0xf bank_mask:0xf
	v_mov_b32_dpp v69, v67 row_ror:4 row_mask:0xf bank_mask:0xf
	v_add_f64 v[66:67], v[66:67], v[68:69]
	s_nop 1
	v_mov_b32_dpp v68, v66 row_ror:2 row_mask:0xf bank_mask:0xf
	v_mov_b32_dpp v69, v67 row_ror:2 row_mask:0xf bank_mask:0xf
	v_add_f64 v[66:67], v[66:67], v[68:69]
	s_nop 1
	v_mov_b32_dpp v68, v66 row_ror:1 row_mask:0xf bank_mask:0xf
	v_mov_b32_dpp v69, v67 row_ror:1 row_mask:0xf bank_mask:0xf
	v_add_f64 v[66:67], v[66:67], v[68:69]
	s_and_saveexec_b64 s[0:1], s[16:17]
	s_cbranch_execz .LBB0_442
	v_lshrrev_b32_e32 v68, 7, v76
	v_and_b32_e32 v68, 0x1fffff8, v68
	v_bfi_b32 v66, s26, v66, v76
	v_add_u32_e32 v68, 0x21c00, v68
	ds_min_u64 v68, v[66:67]
	s_branch .LBB0_442
